# fp8 table conversion loops: the wave's next table row is touched (one dword per lane) while the current row is reduced and converted, so its loads are served from L2
# speedup vs baseline: 1.0630x; 1.0036x over previous
.LBB0_301:
	s_movk_i32 s14, 0x3fff
	v_cmp_lt_i32_e32 vcc, s14, v8
	s_mov_b64 s[18:19], 0
	s_and_saveexec_b64 s[16:17], vcc
	s_xor_b64 s[16:17], exec, s[16:17]
	s_cbranch_execz .LBB0_303
	v_add_u32_e32 v2, 0xffffc000, v8
	v_lshlrev_b64 v[14:15], 12, v[2:3]
	v_lshl_add_u64 v[34:35], v[4:5], 0, v[14:15]
	v_add_u32_e32 v55, s2, v8
	v_cmp_gt_i32_e32 vcc, 0x8000, v55
	v_lshl_add_u64 v[52:53], v[34:35], 0, s[6:7]
	s_nop 0
	v_cndmask_b32_e32 v52, v34, v52, vcc
	v_cndmask_b32_e32 v53, v35, v53, vcc
	global_load_dwordx4 v[14:17], v[34:35], off
	global_load_dwordx4 v[26:29], v[34:35], off offset:16
	global_load_dwordx4 v[30:33], v[34:35], off offset:32
	s_nop 0
	global_load_dwordx4 v[34:37], v[34:35], off offset:48
	global_load_dword v54, v[52:53], off
	v_cmp_lt_i32_e32 vcc, v19, v18
	v_mov_b32_e32 v40, v3
	s_and_b64 s[18:19], s[4:5], exec
	v_cndmask_b32_e32 v25, v1, v19, vcc
	v_lshlrev_b32_e32 v25, 2, v25
	v_cmp_lt_i32_e32 vcc, v20, v18
	s_waitcnt vmcnt(4)
	v_max3_f32 v38, |v14|, 0, |v15|
	v_max3_f32 v38, v38, |v16|, |v17|
	s_waitcnt vmcnt(3)
	v_max3_f32 v38, v38, |v26|, |v27|
	v_max3_f32 v38, v38, |v28|, |v29|
	s_waitcnt vmcnt(2)
	v_max3_f32 v38, v38, |v30|, |v31|
	v_max3_f32 v38, v38, |v32|, |v33|
	s_waitcnt vmcnt(1)
	v_max3_f32 v38, v38, |v34|, |v35|
	v_max3_f32 v38, v38, |v36|, |v37|
	ds_bpermute_b32 v25, v25, v38
	v_cndmask_b32_e32 v39, v1, v20, vcc
	v_lshlrev_b32_e32 v39, 2, v39
	v_cmp_lt_i32_e32 vcc, v21, v18
	s_waitcnt lgkmcnt(0)
	v_max_f32_e32 v25, v25, v25
	v_max_f32_e32 v25, v38, v25
	ds_bpermute_b32 v38, v39, v25
	v_cndmask_b32_e32 v39, v1, v21, vcc
	v_lshlrev_b32_e32 v39, 2, v39
	v_cmp_lt_i32_e32 vcc, v22, v18
	s_waitcnt lgkmcnt(0)
	v_max_f32_e32 v38, v38, v38
	v_max_f32_e32 v25, v25, v38
	ds_bpermute_b32 v38, v39, v25
	v_cndmask_b32_e32 v39, v1, v22, vcc
	v_lshlrev_b32_e32 v39, 2, v39
	v_cmp_lt_i32_e32 vcc, v23, v18
	s_waitcnt lgkmcnt(0)
	v_max_f32_e32 v38, v38, v38
	v_max_f32_e32 v25, v25, v38
	ds_bpermute_b32 v38, v39, v25
	v_cndmask_b32_e32 v39, v1, v23, vcc
	v_lshlrev_b32_e32 v39, 2, v39
	v_cmp_lt_i32_e32 vcc, v24, v18
	s_waitcnt lgkmcnt(0)
	v_max_f32_e32 v38, v38, v38
	v_max_f32_e32 v25, v25, v38
	ds_bpermute_b32 v38, v39, v25
	v_cndmask_b32_e32 v39, v1, v24, vcc
	v_lshlrev_b32_e32 v39, 2, v39
	s_waitcnt lgkmcnt(0)
	v_max_f32_e32 v38, v38, v38
	v_max_f32_e32 v25, v25, v38
	ds_bpermute_b32 v41, v39, v25
	v_mov_b32_e32 v38, v3
	v_mov_b32_e32 v39, v3
	s_waitcnt lgkmcnt(0)
	v_max_f32_e32 v41, v41, v41
	v_max_f32_e32 v25, v25, v41
	v_div_scale_f32 v42, s[14:15], v25, v25, s20
	v_rcp_f32_e32 v43, v42
	v_div_scale_f32 v44, vcc, s20, v25, s20
	v_cmp_lt_f32_e64 s[14:15], 0, v25
	v_fma_f32 v45, -v42, v43, 1.0
	v_fmac_f32_e32 v43, v45, v43
	v_mul_f32_e32 v45, v44, v43
	v_fma_f32 v46, -v42, v45, v44
	v_fmac_f32_e32 v45, v46, v43
	v_fma_f32 v42, -v42, v45, v44
	v_div_fmas_f32 v42, v42, v43, v45
	v_div_fixup_f32 v42, v42, v25, s20
	v_cndmask_b32_e64 v42, 1.0, v42, s[14:15]
	v_mov_b32_e32 v41, v3
	v_mul_f32_e32 v14, v14, v42
	v_mul_f32_e32 v15, v15, v42
	v_mul_f32_e32 v26, v26, v42
	v_mul_f32_e32 v27, v27, v42
	v_mul_f32_e32 v30, v30, v42
	v_mul_f32_e32 v31, v31, v42
	v_mul_f32_e32 v34, v34, v42
	v_mul_f32_e32 v35, v35, v42
	v_cvt_pk_fp8_f32 v38, v14, v15
	v_cvt_pk_fp8_f32 v39, v26, v27
	v_cvt_pk_fp8_f32 v40, v30, v31
	v_cvt_pk_fp8_f32 v41, v34, v35
	v_mul_f32_e32 v16, v16, v42
	v_mul_f32_e32 v17, v17, v42
	v_mul_f32_e32 v28, v28, v42
	v_mul_f32_e32 v29, v29, v42
	v_mul_f32_e32 v32, v32, v42
	v_mul_f32_e32 v33, v33, v42
	v_mul_f32_e32 v36, v36, v42
	v_mul_f32_e32 v37, v37, v42
	v_cvt_pk_fp8_f32 v38, v16, v17 op_sel:[0,0,1]
	v_cvt_pk_fp8_f32 v39, v28, v29 op_sel:[0,0,1]
	v_cvt_pk_fp8_f32 v40, v32, v33 op_sel:[0,0,1]
	v_cvt_pk_fp8_f32 v41, v36, v37 op_sel:[0,0,1]
	v_lshlrev_b64 v[14:15], 10, v[2:3]
	v_lshl_add_u64 v[14:15], v[6:7], 0, v[14:15]
	v_mov_b64_e32 v[16:17], v[2:3]
	global_store_dwordx4 v[14:15], v[38:41], off
.LBB0_303:
	s_or_saveexec_b64 s[16:17], s[16:17]
	v_readlane_b32 s24, v253, 0
	v_readlane_b32 s28, v253, 4
	v_readlane_b32 s29, v253, 5
	v_readlane_b32 s25, v253, 1
	v_readlane_b32 s26, v253, 2
	v_mov_b64_e32 v[14:15], s[28:29]
	v_readlane_b32 s27, v253, 3
	v_readlane_b32 s30, v253, 6
	v_readlane_b32 s31, v253, 7
	s_xor_b64 exec, exec, s[16:17]
	s_cbranch_execz .LBB0_305
	v_add_u32_e32 v55, s2, v8
	v_cmp_gt_i32_e32 vcc, 0x4000, v55
	v_lshl_add_u64 v[52:53], v[10:11], 0, s[6:7]
	s_nop 0
	v_cndmask_b32_e32 v52, v10, v52, vcc
	v_cndmask_b32_e32 v53, v11, v53, vcc
	global_load_dwordx4 v[26:29], v[10:11], off
	global_load_dwordx4 v[30:33], v[10:11], off offset:16
	global_load_dwordx4 v[34:37], v[10:11], off offset:32
	global_load_dwordx4 v[38:41], v[10:11], off offset:48
	global_load_dword v54, v[52:53], off
	v_cmp_lt_i32_e32 vcc, v19, v18
	v_mov_b32_e32 v42, 0
	v_mov_b32_e32 v43, 0
	v_cndmask_b32_e32 v2, v1, v19, vcc
	v_lshlrev_b32_e32 v2, 2, v2
	v_cmp_lt_i32_e32 vcc, v20, v18
	v_mov_b32_e32 v44, 0
	v_mov_b32_e32 v45, 0
	v_cndmask_b32_e32 v15, v1, v20, vcc
	v_lshlrev_b32_e32 v15, 2, v15
	v_cmp_lt_i32_e32 vcc, v21, v18
	v_readlane_b32 s24, v253, 0
	s_andn2_b64 s[18:19], s[18:19], exec
	v_readlane_b32 s26, v253, 2
	v_readlane_b32 s27, v253, 3
	s_andn2_b64 s[14:15], s[14:15], exec
	v_readlane_b32 s25, v253, 1
	v_readlane_b32 s28, v253, 4
	v_readlane_b32 s29, v253, 5
	v_readlane_b32 s30, v253, 6
	v_readlane_b32 s31, v253, 7
	s_waitcnt vmcnt(4)
	v_max3_f32 v14, |v26|, 0, |v27|
	v_max3_f32 v14, v14, |v28|, |v29|
	s_waitcnt vmcnt(3)
	v_max3_f32 v14, v14, |v30|, |v31|
	v_max3_f32 v14, v14, |v32|, |v33|
	s_waitcnt vmcnt(2)
	v_max3_f32 v14, v14, |v34|, |v35|
	v_max3_f32 v14, v14, |v36|, |v37|
	s_waitcnt vmcnt(1)
	v_max3_f32 v14, v14, |v38|, |v39|
	v_max3_f32 v14, v14, |v40|, |v41|
	ds_bpermute_b32 v2, v2, v14
	s_waitcnt lgkmcnt(0)
	v_max_f32_e32 v2, v2, v2
	v_max_f32_e32 v2, v14, v2
	ds_bpermute_b32 v14, v15, v2
	v_cndmask_b32_e32 v15, v1, v21, vcc
	v_lshlrev_b32_e32 v15, 2, v15
	v_cmp_lt_i32_e32 vcc, v22, v18
	s_waitcnt lgkmcnt(0)
	v_max_f32_e32 v14, v14, v14
	v_max_f32_e32 v2, v2, v14
	ds_bpermute_b32 v14, v15, v2
	v_cndmask_b32_e32 v15, v1, v22, vcc
	v_lshlrev_b32_e32 v15, 2, v15
	v_cmp_lt_i32_e32 vcc, v23, v18
	s_waitcnt lgkmcnt(0)
	v_max_f32_e32 v14, v14, v14
	v_max_f32_e32 v2, v2, v14
	ds_bpermute_b32 v14, v15, v2
	v_cndmask_b32_e32 v15, v1, v23, vcc
	v_lshlrev_b32_e32 v15, 2, v15
	v_cmp_lt_i32_e32 vcc, v24, v18
	s_waitcnt lgkmcnt(0)
	v_max_f32_e32 v14, v14, v14
	v_max_f32_e32 v2, v2, v14
	ds_bpermute_b32 v14, v15, v2
	v_cndmask_b32_e32 v16, v1, v24, vcc
	v_lshlrev_b32_e32 v15, 2, v16
	s_waitcnt lgkmcnt(0)
	v_max_f32_e32 v14, v14, v14
	v_max_f32_e32 v2, v2, v14
	ds_bpermute_b32 v16, v15, v2
	v_mov_b64_e32 v[14:15], s[26:27]
	s_waitcnt lgkmcnt(0)
	v_max_f32_e32 v16, v16, v16
	v_max_f32_e32 v25, v2, v16
	v_div_scale_f32 v2, s[22:23], v25, v25, s20
	v_rcp_f32_e32 v16, v2
	v_div_scale_f32 v17, vcc, s20, v25, s20
	s_and_b64 s[22:23], s[4:5], exec
	v_fma_f32 v46, -v2, v16, 1.0
	v_fmac_f32_e32 v16, v46, v16
	v_mul_f32_e32 v46, v17, v16
	v_fma_f32 v47, -v2, v46, v17
	v_fmac_f32_e32 v46, v47, v16
	v_fma_f32 v2, -v2, v46, v17
	v_div_fmas_f32 v2, v2, v16, v46
	v_div_fixup_f32 v2, v2, v25, s20
	v_cmp_lt_f32_e32 vcc, 0, v25
	s_or_b64 s[18:19], s[18:19], s[22:23]
	s_and_b64 s[22:23], vcc, exec
	v_cndmask_b32_e32 v2, 1.0, v2, vcc
	v_mul_f32_e32 v16, v26, v2
	v_mul_f32_e32 v17, v27, v2
	v_mul_f32_e32 v26, v28, v2
	v_mul_f32_e32 v27, v29, v2
	v_mul_f32_e32 v28, v30, v2
	v_mul_f32_e32 v29, v31, v2
	v_mul_f32_e32 v30, v32, v2
	v_mul_f32_e32 v31, v33, v2
	v_mul_f32_e32 v32, v34, v2
	v_mul_f32_e32 v33, v35, v2
	v_mul_f32_e32 v34, v36, v2
	v_mul_f32_e32 v35, v37, v2
	v_mul_f32_e32 v36, v38, v2
	v_mul_f32_e32 v37, v39, v2
	v_cvt_pk_fp8_f32 v42, v16, v17
	v_cvt_pk_fp8_f32 v43, v28, v29
	v_cvt_pk_fp8_f32 v44, v32, v33
	v_cvt_pk_fp8_f32 v45, v36, v37
	v_mul_f32_e32 v38, v40, v2
	v_mul_f32_e32 v2, v41, v2
	v_cvt_pk_fp8_f32 v42, v26, v27 op_sel:[0,0,1]
	v_cvt_pk_fp8_f32 v43, v30, v31 op_sel:[0,0,1]
	v_cvt_pk_fp8_f32 v44, v34, v35 op_sel:[0,0,1]
	v_cvt_pk_fp8_f32 v45, v38, v2 op_sel:[0,0,1]
	s_or_b64 s[14:15], s[14:15], s[22:23]
	v_mov_b64_e32 v[16:17], v[8:9]
	global_store_dwordx4 v[12:13], v[42:45], off

.LBB0_457:
	s_movk_i32 s2, 0x3fff
	v_cmp_lt_i32_e32 vcc, s2, v28
	s_mov_b64 s[20:21], 0
	s_and_saveexec_b64 s[2:3], vcc
	s_xor_b64 s[16:17], exec, s[2:3]
	s_cbranch_execz .LBB0_459
	v_add_u32_e32 v2, 0xffffc000, v28
	v_lshlrev_b64 v[4:5], 12, v[2:3]
	v_lshl_add_u64 v[16:17], v[24:25], 0, v[4:5]
	v_add_u32_e32 v55, s6, v28
	v_cmp_gt_i32_e32 vcc, 0x8000, v55
	v_lshl_add_u64 v[52:53], v[16:17], 0, s[10:11]
	s_nop 0
	v_cndmask_b32_e32 v52, v16, v52, vcc
	v_cndmask_b32_e32 v53, v17, v53, vcc
	global_load_dwordx4 v[4:7], v[16:17], off
	global_load_dwordx4 v[8:11], v[16:17], off offset:16
	global_load_dwordx4 v[12:15], v[16:17], off offset:32
	s_nop 0
	global_load_dwordx4 v[16:19], v[16:17], off offset:48
	global_load_dword v54, v[52:53], off
	v_mbcnt_hi_u32_b32 v1, -1, v197
	v_and_b32_e32 v20, 64, v1
	v_xor_b32_e32 v21, 1, v1
	v_add_u32_e32 v20, 64, v20
	v_cmp_lt_i32_e32 vcc, v21, v20
	v_xor_b32_e32 v23, 2, v1
	s_and_b64 s[20:21], s[4:5], exec
	v_cndmask_b32_e32 v21, v1, v21, vcc
	v_lshlrev_b32_e32 v21, 2, v21
	v_cmp_lt_i32_e32 vcc, v23, v20
	s_waitcnt vmcnt(4)
	v_max3_f32 v22, |v4|, 0, |v5|
	v_max3_f32 v22, v22, |v6|, |v7|
	s_waitcnt vmcnt(3)
	v_max3_f32 v22, v22, |v8|, |v9|
	v_max3_f32 v22, v22, |v10|, |v11|
	s_waitcnt vmcnt(2)
	v_max3_f32 v22, v22, |v12|, |v13|
	v_max3_f32 v22, v22, |v14|, |v15|
	s_waitcnt vmcnt(1)
	v_max3_f32 v22, v22, |v16|, |v17|
	v_max3_f32 v22, v22, |v18|, |v19|
	ds_bpermute_b32 v21, v21, v22
	v_cndmask_b32_e32 v23, v1, v23, vcc
	v_lshlrev_b32_e32 v23, 2, v23
	s_waitcnt lgkmcnt(0)
	v_max_f32_e32 v21, v21, v21
	v_max_f32_e32 v21, v22, v21
	ds_bpermute_b32 v22, v23, v21
	v_xor_b32_e32 v23, 4, v1
	v_cmp_lt_i32_e32 vcc, v23, v20
	s_waitcnt lgkmcnt(0)
	v_max_f32_e32 v22, v22, v22
	v_cndmask_b32_e32 v23, v1, v23, vcc
	v_lshlrev_b32_e32 v23, 2, v23
	v_max_f32_e32 v21, v21, v22
	ds_bpermute_b32 v22, v23, v21
	v_xor_b32_e32 v23, 8, v1
	v_cmp_lt_i32_e32 vcc, v23, v20
	s_waitcnt lgkmcnt(0)
	v_max_f32_e32 v22, v22, v22
	v_cndmask_b32_e32 v23, v1, v23, vcc
	v_lshlrev_b32_e32 v23, 2, v23
	v_max_f32_e32 v21, v21, v22
	ds_bpermute_b32 v22, v23, v21
	v_xor_b32_e32 v23, 16, v1
	v_cmp_lt_i32_e32 vcc, v23, v20
	s_waitcnt lgkmcnt(0)
	v_max_f32_e32 v22, v22, v22
	v_cndmask_b32_e32 v23, v1, v23, vcc
	v_lshlrev_b32_e32 v23, 2, v23
	v_max_f32_e32 v21, v21, v22
	ds_bpermute_b32 v22, v23, v21
	v_xor_b32_e32 v23, 32, v1
	v_cmp_lt_i32_e32 vcc, v23, v20
	s_waitcnt lgkmcnt(0)
	v_max_f32_e32 v20, v22, v22
	v_cndmask_b32_e32 v1, v1, v23, vcc
	v_lshlrev_b32_e32 v1, 2, v1
	v_max_f32_e32 v23, v21, v20
	ds_bpermute_b32 v1, v1, v23
	v_mov_b32_e32 v20, v3
	v_mov_b32_e32 v21, v3
	v_mov_b32_e32 v22, v3
	s_waitcnt lgkmcnt(0)
	v_max_f32_e32 v1, v1, v1
	v_max_f32_e32 v1, v23, v1
	v_div_scale_f32 v34, s[2:3], v1, v1, s86
	v_rcp_f32_e32 v35, v34
	v_div_scale_f32 v36, vcc, s86, v1, s86
	v_cmp_lt_f32_e64 s[14:15], 0, v1
	v_fma_f32 v37, -v34, v35, 1.0
	v_fmac_f32_e32 v35, v37, v35
	v_mul_f32_e32 v37, v36, v35
	v_fma_f32 v38, -v34, v37, v36
	v_fmac_f32_e32 v37, v38, v35
	v_fma_f32 v34, -v34, v37, v36
	v_div_fmas_f32 v34, v34, v35, v37
	v_div_fixup_f32 v34, v34, v1, s86
	v_cndmask_b32_e64 v34, 1.0, v34, s[14:15]
	v_mov_b32_e32 v23, v3
	v_mul_f32_e32 v4, v4, v34
	v_mul_f32_e32 v5, v5, v34
	v_mul_f32_e32 v8, v8, v34
	v_mul_f32_e32 v9, v9, v34
	v_mul_f32_e32 v12, v12, v34
	v_mul_f32_e32 v13, v13, v34
	v_mul_f32_e32 v16, v16, v34
	v_mul_f32_e32 v17, v17, v34
	v_cvt_pk_fp8_f32 v20, v4, v5
	v_cvt_pk_fp8_f32 v21, v8, v9
	v_cvt_pk_fp8_f32 v22, v12, v13
	v_cvt_pk_fp8_f32 v23, v16, v17
	v_mul_f32_e32 v6, v6, v34
	v_mul_f32_e32 v7, v7, v34
	v_mul_f32_e32 v10, v10, v34
	v_mul_f32_e32 v11, v11, v34
	v_mul_f32_e32 v14, v14, v34
	v_mul_f32_e32 v15, v15, v34
	v_mul_f32_e32 v18, v18, v34
	v_mul_f32_e32 v19, v19, v34
	v_cvt_pk_fp8_f32 v20, v6, v7 op_sel:[0,0,1]
	v_cvt_pk_fp8_f32 v21, v10, v11 op_sel:[0,0,1]
	v_cvt_pk_fp8_f32 v22, v14, v15 op_sel:[0,0,1]
	v_cvt_pk_fp8_f32 v23, v18, v19 op_sel:[0,0,1]
	v_lshlrev_b64 v[4:5], 10, v[2:3]
	v_lshl_add_u64 v[4:5], v[26:27], 0, v[4:5]
	global_store_dwordx4 v[4:5], v[20:23], off
	v_mov_b64_e32 v[4:5], v[2:3]
.LBB0_459:
	s_or_saveexec_b64 s[16:17], s[16:17]
	v_readlane_b32 s24, v253, 0
	v_readlane_b32 s28, v253, 4
	v_readlane_b32 s29, v253, 5
	v_readlane_b32 s25, v253, 1
	v_readlane_b32 s26, v253, 2
	v_mov_b64_e32 v[34:35], s[28:29]
	v_readlane_b32 s27, v253, 3
	v_readlane_b32 s30, v253, 6
	v_readlane_b32 s31, v253, 7
	s_xor_b64 exec, exec, s[16:17]
	s_cbranch_execz .LBB0_461
	v_add_u32_e32 v55, s6, v28
	v_cmp_gt_i32_e32 vcc, 0x4000, v55
	v_lshl_add_u64 v[52:53], v[32:33], 0, s[10:11]
	s_nop 0
	v_cndmask_b32_e32 v52, v32, v52, vcc
	v_cndmask_b32_e32 v53, v33, v53, vcc
	global_load_dwordx4 v[16:19], v[32:33], off offset:-32
	global_load_dwordx4 v[12:15], v[32:33], off offset:-16
	global_load_dwordx4 v[8:11], v[32:33], off
	global_load_dwordx4 v[4:7], v[32:33], off offset:16
	global_load_dword v54, v[52:53], off
	v_mbcnt_hi_u32_b32 v1, -1, v197
	v_and_b32_e32 v2, 64, v1
	v_xor_b32_e32 v23, 1, v1
	v_add_u32_e32 v2, 64, v2
	v_cmp_lt_i32_e32 vcc, v23, v2
	v_xor_b32_e32 v35, 2, v1
	s_andn2_b64 s[2:3], s[14:15], exec
	v_cndmask_b32_e32 v23, v1, v23, vcc
	v_lshlrev_b32_e32 v23, 2, v23
	v_cmp_lt_i32_e32 vcc, v35, v2
	s_andn2_b64 s[14:15], s[20:21], exec
	v_mov_b32_e32 v20, v3
	v_cndmask_b32_e32 v35, v1, v35, vcc
	v_lshlrev_b32_e32 v35, 2, v35
	v_mov_b32_e32 v21, v3
	v_mov_b32_e32 v22, v3
	v_readlane_b32 s24, v253, 0
	v_readlane_b32 s26, v253, 2
	v_readlane_b32 s27, v253, 3
	v_readlane_b32 s25, v253, 1
	v_readlane_b32 s28, v253, 4
	v_readlane_b32 s29, v253, 5
	v_readlane_b32 s30, v253, 6
	v_readlane_b32 s31, v253, 7
	s_waitcnt vmcnt(4)
	v_max3_f32 v34, |v16|, 0, |v17|
	v_max3_f32 v34, v34, |v18|, |v19|
	s_waitcnt vmcnt(3)
	v_max3_f32 v34, v34, |v12|, |v13|
	v_max3_f32 v34, v34, |v14|, |v15|
	s_waitcnt vmcnt(2)
	v_max3_f32 v34, v34, |v8|, |v9|
	v_max3_f32 v34, v34, |v10|, |v11|
	s_waitcnt vmcnt(1)
	v_max3_f32 v34, v34, |v4|, |v5|
	v_max3_f32 v34, v34, |v6|, |v7|
	ds_bpermute_b32 v23, v23, v34
	s_waitcnt lgkmcnt(0)
	v_max_f32_e32 v23, v23, v23
	v_max_f32_e32 v23, v34, v23
	ds_bpermute_b32 v34, v35, v23
	v_xor_b32_e32 v35, 4, v1
	v_cmp_lt_i32_e32 vcc, v35, v2
	s_waitcnt lgkmcnt(0)
	v_max_f32_e32 v34, v34, v34
	v_cndmask_b32_e32 v35, v1, v35, vcc
	v_lshlrev_b32_e32 v35, 2, v35
	v_max_f32_e32 v23, v23, v34
	ds_bpermute_b32 v34, v35, v23
	v_xor_b32_e32 v35, 8, v1
	v_cmp_lt_i32_e32 vcc, v35, v2
	s_waitcnt lgkmcnt(0)
	v_max_f32_e32 v34, v34, v34
	v_cndmask_b32_e32 v35, v1, v35, vcc
	v_lshlrev_b32_e32 v35, 2, v35
	v_max_f32_e32 v23, v23, v34
	ds_bpermute_b32 v34, v35, v23
	v_xor_b32_e32 v35, 16, v1
	v_cmp_lt_i32_e32 vcc, v35, v2
	s_waitcnt lgkmcnt(0)
	v_max_f32_e32 v34, v34, v34
	v_cndmask_b32_e32 v35, v1, v35, vcc
	v_lshlrev_b32_e32 v35, 2, v35
	v_max_f32_e32 v23, v23, v34
	ds_bpermute_b32 v34, v35, v23
	v_xor_b32_e32 v35, 32, v1
	v_cmp_lt_i32_e32 vcc, v35, v2
	s_waitcnt lgkmcnt(0)
	v_max_f32_e32 v2, v34, v34
	v_cndmask_b32_e32 v1, v1, v35, vcc
	v_lshlrev_b32_e32 v1, 2, v1
	v_max_f32_e32 v2, v23, v2
	ds_bpermute_b32 v1, v1, v2
	v_mov_b32_e32 v23, v3
	v_mov_b64_e32 v[34:35], s[26:27]
	s_waitcnt lgkmcnt(0)
	v_max_f32_e32 v1, v1, v1
	v_max_f32_e32 v1, v2, v1
	v_div_scale_f32 v2, s[20:21], v1, v1, s86
	v_rcp_f32_e32 v36, v2
	v_div_scale_f32 v37, vcc, s86, v1, s86
	s_and_b64 s[20:21], s[4:5], exec
	v_fma_f32 v38, -v2, v36, 1.0
	v_fmac_f32_e32 v36, v38, v36
	v_mul_f32_e32 v38, v37, v36
	v_fma_f32 v39, -v2, v38, v37
	v_fmac_f32_e32 v38, v39, v36
	v_fma_f32 v2, -v2, v38, v37
	v_div_fmas_f32 v2, v2, v36, v38
	v_div_fixup_f32 v2, v2, v1, s86
	v_cmp_lt_f32_e32 vcc, 0, v1
	s_or_b64 s[20:21], s[14:15], s[20:21]
	s_and_b64 s[14:15], vcc, exec
	v_cndmask_b32_e32 v2, 1.0, v2, vcc
	v_mul_f32_e32 v16, v16, v2
	v_mul_f32_e32 v17, v17, v2
	v_mul_f32_e32 v12, v12, v2
	v_mul_f32_e32 v13, v13, v2
	v_mul_f32_e32 v8, v8, v2
	v_mul_f32_e32 v9, v9, v2
	v_mul_f32_e32 v4, v4, v2
	v_mul_f32_e32 v5, v5, v2
	v_cvt_pk_fp8_f32 v20, v16, v17
	v_cvt_pk_fp8_f32 v21, v12, v13
	v_cvt_pk_fp8_f32 v22, v8, v9
	v_cvt_pk_fp8_f32 v23, v4, v5
	v_mul_f32_e32 v18, v18, v2
	v_mul_f32_e32 v19, v19, v2
	v_mul_f32_e32 v14, v14, v2
	v_mul_f32_e32 v15, v15, v2
	v_mul_f32_e32 v10, v10, v2
	v_mul_f32_e32 v11, v11, v2
	v_mul_f32_e32 v6, v6, v2
	v_mul_f32_e32 v2, v7, v2
	v_cvt_pk_fp8_f32 v20, v18, v19 op_sel:[0,0,1]
	v_cvt_pk_fp8_f32 v21, v14, v15 op_sel:[0,0,1]
	v_cvt_pk_fp8_f32 v22, v10, v11 op_sel:[0,0,1]
	v_cvt_pk_fp8_f32 v23, v6, v2 op_sel:[0,0,1]
	s_or_b64 s[14:15], s[2:3], s[14:15]
	v_mov_b64_e32 v[4:5], v[28:29]
	global_store_dwordx4 v[30:31], v[20:23], off
